# v038 + nt policy on the GU epilogue HID stores (not re-read until the next phase)
# baseline (speedup 1.0000x reference)
; __device__ __forceinline__ float silu_fast(float v) { return v * __builtin_amdgcn_rcpf(1.f + __builtin_amdgcn_exp2f(-1.4426950408889634f * v)); }
; __device__ __forceinline__ u32x4 pack8(const f32x4 a, const f32x4 b) { u32x4 w; w.x = cvt_pk_bf16(a[0], a[1]); w.y = cvt_pk_bf16(a[2], a[3]); w.z = cvt_pk_bf16(b[0], b[1]); w.w = cvt_pk_bf16(b[2], b[3]); return w; }
;     __device__ __forceinline__ void operator()(const f32x4 (&acc)[2][2][4][2], const Unit& u, int wr, int wc, int fr, int fq) const {
;         const int row0 = u.pm * BM + wr * 64 + fr, col0 = u.pn * HALF + wc * 32 + 8 * fq;
;         bf16_t* base = HID + (size_t)u.z * MEXP * FF;
; #pragma unroll
;         for (int ai = 0; ai < 2; ++ai)
; #pragma unroll
;             for (int m = 0; m < 4; ++m) { f32x4 h[2];
; #pragma unroll
;                 for (int n = 0; n < 2; ++n)
; #pragma unroll
;                     for (int j = 0; j < 4; ++j) h[n][j] = silu_fast(acc[ai][0][m][n][j]) * acc[ai][1][m][n][j];
;                 const int row = row0 + ai * HALF + m * 16;
;                 *(u32x4*)(base + ((size_t)(row >> 7) * (FF / 64) + (col0 >> 6)) * 8192 + (row & 127) * 64 + (col0 & 63)) = pack8(h[0], h[1]); }
;     }
.LBB0_1018:
	v_mul_f32_e32 v2, 0xbfb8aa3b, v130
	v_exp_f32_e32 v2, v2
	v_mul_f32_e32 v136, 0xbfb8aa3b, v131
	v_exp_f32_e32 v136, v136
	s_lshl_b32 s6, s63, 8
	v_add_f32_e32 v2, 1.0, v2
	v_rcp_f32_e32 v138, v2
	v_add_f32_e32 v2, 1.0, v136
	v_rcp_f32_e32 v139, v2
	v_mul_f32_e32 v2, 0xbfb8aa3b, v132
	v_exp_f32_e32 v2, v2
	s_add_i32 s6, s6, s45
	v_pk_mul_f32 v[130:131], v[130:131], v[138:139]
	v_mul_f32_e32 v138, 0xbfb8aa3b, v133
	v_exp_f32_e32 v138, v138
	v_add_f32_e32 v2, 1.0, v2
	v_pk_mul_f32 v[122:123], v[122:123], v[130:131]
	v_rcp_f32_e32 v130, v2
	v_add_f32_e32 v2, 1.0, v138
	v_rcp_f32_e32 v131, v2
	v_mul_f32_e32 v2, 0xbfb8aa3b, v126
	v_exp_f32_e32 v2, v2
	v_mul_f32_e32 v138, 0xbfb8aa3b, v127
	v_exp_f32_e32 v138, v138
	v_pk_mul_f32 v[130:131], v[132:133], v[130:131]
	v_add_f32_e32 v2, 1.0, v2
	v_mul_f32_e32 v133, 0xbfb8aa3b, v128
	v_rcp_f32_e32 v132, v2
	v_add_f32_e32 v2, 1.0, v138
	v_exp_f32_e32 v138, v133
	v_mul_f32_e32 v133, 0xbfb8aa3b, v129
	v_exp_f32_e32 v139, v133
	v_rcp_f32_e32 v133, v2
	v_add_f32_e32 v2, 1.0, v138
	v_rcp_f32_e32 v138, v2
	v_add_f32_e32 v2, 1.0, v139
	v_rcp_f32_e32 v139, v2
	s_lshl_b32 s4, s22, 7
	v_pk_mul_f32 v[126:127], v[126:127], v[132:133]
	s_or_b32 s4, s4, s46
	s_ashr_i32 s7, s6, 7
	v_pk_mul_f32 v[126:127], v[118:119], v[126:127]
	v_pk_mul_f32 v[118:119], v[128:129], v[138:139]
	v_mul_f32_e32 v2, 0xbfb8aa3b, v114
	s_ashr_i32 s5, s4, 6
	v_mad_i64_i32 v[134:135], s[8:9], s62, v230, v[206:207]
	s_mul_i32 s7, s7, 44
	v_pk_mul_f32 v[128:129], v[120:121], v[118:119]
	v_exp_f32_e32 v2, v2
	v_mul_f32_e32 v121, 0xbfb8aa3b, v115
	s_ashr_i32 s4, s5, 31
	s_ashr_i32 s9, s7, 31
	v_cvt_pk_bf16_f32 v118, v122, v123
	v_exp_f32_e32 v123, v121
	s_add_u32 s8, s7, s5
	s_addc_u32 s9, s9, s4
	s_lshl_b64 s[8:9], s[8:9], 14
	v_add_f32_e32 v2, 1.0, v2
	v_lshl_add_u64 v[136:137], v[134:135], 0, s[8:9]
	v_pk_mul_f32 v[124:125], v[124:125], v[130:131]
	v_rcp_f32_e32 v122, v2
	v_add_f32_e32 v2, 1.0, v123
	v_mov_b32_e32 v209, v3
	v_cvt_pk_bf16_f32 v119, v124, v125
	v_cvt_pk_bf16_f32 v120, v126, v127
	v_cvt_pk_bf16_f32 v121, v128, v129
	v_rcp_f32_e32 v123, v2
	v_lshl_add_u64 v[124:125], v[136:137], 0, v[208:209]
	v_mul_f32_e32 v2, 0xbfb8aa3b, v116
	global_store_dwordx4 v[124:125], v[118:121], off nt
	v_exp_f32_e32 v2, v2
	v_pk_mul_f32 v[114:115], v[114:115], v[122:123]
	v_mul_f32_e32 v118, 0xbfb8aa3b, v117
	v_exp_f32_e32 v118, v118
	v_add_f32_e32 v2, 1.0, v2
	v_pk_mul_f32 v[106:107], v[106:107], v[114:115]
	v_rcp_f32_e32 v114, v2
	v_add_f32_e32 v2, 1.0, v118
	v_rcp_f32_e32 v115, v2
	v_mul_f32_e32 v2, 0xbfb8aa3b, v110
	v_exp_f32_e32 v2, v2
	v_mul_f32_e32 v118, 0xbfb8aa3b, v111
	v_exp_f32_e32 v118, v118
	v_pk_mul_f32 v[114:115], v[116:117], v[114:115]
	v_add_f32_e32 v2, 1.0, v2
	v_mul_f32_e32 v117, 0xbfb8aa3b, v112
	v_rcp_f32_e32 v116, v2
	v_add_f32_e32 v2, 1.0, v118
	v_exp_f32_e32 v118, v117
	v_mul_f32_e32 v117, 0xbfb8aa3b, v113
	v_exp_f32_e32 v119, v117
	v_rcp_f32_e32 v117, v2
	v_add_f32_e32 v2, 1.0, v118
	v_rcp_f32_e32 v118, v2
	v_add_f32_e32 v2, 1.0, v119
	v_rcp_f32_e32 v119, v2
	v_pk_mul_f32 v[110:111], v[110:111], v[116:117]
	v_mul_f32_e32 v2, 0xbfb8aa3b, v98
	v_pk_mul_f32 v[110:111], v[102:103], v[110:111]
	v_pk_mul_f32 v[102:103], v[112:113], v[118:119]
	v_exp_f32_e32 v2, v2
	v_pk_mul_f32 v[112:113], v[104:105], v[102:103]
	v_mul_f32_e32 v103, 0xbfb8aa3b, v99
	v_exp_f32_e32 v104, v103
	v_add_f32_e32 v2, 1.0, v2
	v_pk_mul_f32 v[108:109], v[108:109], v[114:115]
	v_cvt_pk_bf16_f32 v102, v106, v107
	v_rcp_f32_e32 v106, v2
	v_add_f32_e32 v2, 1.0, v104
	v_cvt_pk_bf16_f32 v103, v108, v109
	v_rcp_f32_e32 v107, v2
	v_cvt_pk_bf16_f32 v104, v110, v111
	v_cvt_pk_bf16_f32 v105, v112, v113
	v_mul_f32_e32 v2, 0xbfb8aa3b, v100
	global_store_dwordx4 v[124:125], v[102:105], off offset:2048 nt
	v_exp_f32_e32 v2, v2
	v_pk_mul_f32 v[98:99], v[98:99], v[106:107]
	v_mul_f32_e32 v102, 0xbfb8aa3b, v101
	v_exp_f32_e32 v102, v102
	v_add_f32_e32 v2, 1.0, v2
	v_pk_mul_f32 v[90:91], v[90:91], v[98:99]
	v_rcp_f32_e32 v98, v2
	v_add_f32_e32 v2, 1.0, v102
	v_rcp_f32_e32 v99, v2
	v_mul_f32_e32 v2, 0xbfb8aa3b, v94
	v_exp_f32_e32 v2, v2
	v_mul_f32_e32 v102, 0xbfb8aa3b, v95
	v_exp_f32_e32 v102, v102
	v_pk_mul_f32 v[98:99], v[100:101], v[98:99]
	v_add_f32_e32 v2, 1.0, v2
	v_mul_f32_e32 v101, 0xbfb8aa3b, v96
	v_rcp_f32_e32 v100, v2
	v_add_f32_e32 v2, 1.0, v102
	v_exp_f32_e32 v102, v101
	v_mul_f32_e32 v101, 0xbfb8aa3b, v97
	v_exp_f32_e32 v103, v101
	v_rcp_f32_e32 v101, v2
	v_add_f32_e32 v2, 1.0, v102
	v_rcp_f32_e32 v102, v2
	v_add_f32_e32 v2, 1.0, v103
	v_rcp_f32_e32 v103, v2
	v_pk_mul_f32 v[94:95], v[94:95], v[100:101]
	v_mul_f32_e32 v2, 0xbfb8aa3b, v82
	v_pk_mul_f32 v[94:95], v[86:87], v[94:95]
	v_pk_mul_f32 v[86:87], v[96:97], v[102:103]
	v_exp_f32_e32 v2, v2
	v_pk_mul_f32 v[96:97], v[88:89], v[86:87]
	v_mul_f32_e32 v89, 0xbfb8aa3b, v83
	v_cvt_pk_bf16_f32 v86, v90, v91
	v_exp_f32_e32 v91, v89
	v_add_f32_e32 v2, 1.0, v2
	v_pk_mul_f32 v[92:93], v[92:93], v[98:99]
	v_rcp_f32_e32 v90, v2
	v_add_f32_e32 v2, 1.0, v91
	v_mov_b32_e32 v211, v3
	v_cvt_pk_bf16_f32 v87, v92, v93
	v_cvt_pk_bf16_f32 v88, v94, v95
	v_cvt_pk_bf16_f32 v89, v96, v97
	v_rcp_f32_e32 v91, v2
	v_lshl_add_u64 v[92:93], v[136:137], 0, v[210:211]
	v_mul_f32_e32 v2, 0xbfb8aa3b, v84
	global_store_dwordx4 v[92:93], v[86:89], off nt
	v_exp_f32_e32 v2, v2
	v_pk_mul_f32 v[82:83], v[82:83], v[90:91]
	v_mul_f32_e32 v86, 0xbfb8aa3b, v85
	v_exp_f32_e32 v86, v86
	v_add_f32_e32 v2, 1.0, v2
	v_pk_mul_f32 v[74:75], v[74:75], v[82:83]
	v_rcp_f32_e32 v82, v2
	v_add_f32_e32 v2, 1.0, v86
	v_rcp_f32_e32 v83, v2
	v_mul_f32_e32 v2, 0xbfb8aa3b, v78
	v_exp_f32_e32 v2, v2
	v_mul_f32_e32 v86, 0xbfb8aa3b, v79
	v_exp_f32_e32 v86, v86
; __device__ __forceinline__ float silu_fast(float v) { return v * __builtin_amdgcn_rcpf(1.f + __builtin_amdgcn_exp2f(-1.4426950408889634f * v)); }
; __device__ __forceinline__ u32x4 pack8(const f32x4 a, const f32x4 b) { u32x4 w; w.x = cvt_pk_bf16(a[0], a[1]); w.y = cvt_pk_bf16(a[2], a[3]); w.z = cvt_pk_bf16(b[0], b[1]); w.w = cvt_pk_bf16(b[2], b[3]); return w; }
;     __device__ __forceinline__ void operator()(const f32x4 (&acc)[2][2][4][2], const Unit& u, int wr, int wc, int fr, int fq) const {
;     ...
;         for (int ai = 0; ai < 2; ++ai)
; #pragma unroll
;             for (int m = 0; m < 4; ++m) { f32x4 h[2];
; #pragma unroll
;                 for (int n = 0; n < 2; ++n)
; #pragma unroll
;                     for (int j = 0; j < 4; ++j) h[n][j] = silu_fast(acc[ai][0][m][n][j]) * acc[ai][1][m][n][j];
;                 const int row = row0 + ai * HALF + m * 16;
;                 *(u32x4*)(base + ((size_t)(row >> 7) * (FF / 64) + (col0 >> 6)) * 8192 + (row & 127) * 64 + (col0 & 63)) = pack8(h[0], h[1]); }
;     }
	v_pk_mul_f32 v[82:83], v[84:85], v[82:83]
	v_add_f32_e32 v2, 1.0, v2
	v_mul_f32_e32 v85, 0xbfb8aa3b, v80
	v_rcp_f32_e32 v84, v2
	v_add_f32_e32 v2, 1.0, v86
	v_exp_f32_e32 v86, v85
	v_mul_f32_e32 v85, 0xbfb8aa3b, v81
	v_exp_f32_e32 v87, v85
	v_rcp_f32_e32 v85, v2
	v_add_f32_e32 v2, 1.0, v86
	v_rcp_f32_e32 v86, v2
	v_add_f32_e32 v2, 1.0, v87
	v_rcp_f32_e32 v87, v2
	v_pk_mul_f32 v[78:79], v[78:79], v[84:85]
	v_pk_mul_f32 v[76:77], v[76:77], v[82:83]
	v_pk_mul_f32 v[78:79], v[70:71], v[78:79]
	v_pk_mul_f32 v[70:71], v[80:81], v[86:87]
	v_mov_b32_e32 v213, v3
	v_pk_mul_f32 v[80:81], v[72:73], v[70:71]
	v_cvt_pk_bf16_f32 v70, v74, v75
	v_cvt_pk_bf16_f32 v71, v76, v77
	v_cvt_pk_bf16_f32 v72, v78, v79
	v_cvt_pk_bf16_f32 v73, v80, v81
	v_lshl_add_u64 v[74:75], v[136:137], 0, v[212:213]
	v_mul_f32_e32 v2, 0xbfb8aa3b, v66
	global_store_dwordx4 v[74:75], v[70:73], off nt
	v_exp_f32_e32 v2, v2
	s_addk_i32 s6, 0x80
	v_mul_f32_e32 v70, 0xbfb8aa3b, v67
	v_exp_f32_e32 v70, v70
	v_add_f32_e32 v2, 1.0, v2
	v_rcp_f32_e32 v72, v2
	s_ashr_i32 s6, s6, 7
	v_add_f32_e32 v2, 1.0, v70
	v_rcp_f32_e32 v73, v2
	v_mul_f32_e32 v2, 0xbfb8aa3b, v68
	v_exp_f32_e32 v2, v2
	s_mul_i32 s6, s6, 44
	v_pk_mul_f32 v[66:67], v[66:67], v[72:73]
	v_mul_f32_e32 v72, 0xbfb8aa3b, v69
	v_exp_f32_e32 v72, v72
	v_add_f32_e32 v2, 1.0, v2
	v_pk_mul_f32 v[58:59], v[58:59], v[66:67]
	v_rcp_f32_e32 v66, v2
	v_add_f32_e32 v2, 1.0, v72
	v_rcp_f32_e32 v67, v2
	v_mul_f32_e32 v2, 0xbfb8aa3b, v62
	v_exp_f32_e32 v2, v2
	v_mul_f32_e32 v72, 0xbfb8aa3b, v63
	v_exp_f32_e32 v72, v72
	v_pk_mul_f32 v[66:67], v[68:69], v[66:67]
	v_add_f32_e32 v2, 1.0, v2
	v_mul_f32_e32 v69, 0xbfb8aa3b, v64
	v_rcp_f32_e32 v68, v2
	v_add_f32_e32 v2, 1.0, v72
	v_exp_f32_e32 v72, v69
	v_mul_f32_e32 v69, 0xbfb8aa3b, v65
	v_exp_f32_e32 v73, v69
	v_rcp_f32_e32 v69, v2
	v_add_f32_e32 v2, 1.0, v72
	v_rcp_f32_e32 v72, v2
	v_add_f32_e32 v2, 1.0, v73
	v_rcp_f32_e32 v73, v2
	v_pk_mul_f32 v[62:63], v[62:63], v[68:69]
	v_mul_f32_e32 v2, 0xbfb8aa3b, v50
	v_pk_mul_f32 v[62:63], v[54:55], v[62:63]
	v_pk_mul_f32 v[54:55], v[64:65], v[72:73]
	v_exp_f32_e32 v2, v2
	v_pk_mul_f32 v[64:65], v[56:57], v[54:55]
	v_mul_f32_e32 v56, 0xbfb8aa3b, v51
	s_ashr_i32 s7, s6, 31
	v_exp_f32_e32 v57, v56
	s_add_u32 s6, s6, s5
	s_addc_u32 s7, s7, s4
	s_lshl_b64 s[4:5], s[6:7], 14
	v_add_f32_e32 v2, 1.0, v2
	v_lshl_add_u64 v[70:71], v[134:135], 0, s[4:5]
	v_pk_mul_f32 v[60:61], v[60:61], v[66:67]
	v_cvt_pk_bf16_f32 v54, v58, v59
	v_rcp_f32_e32 v58, v2
	v_add_f32_e32 v2, 1.0, v57
	v_cvt_pk_bf16_f32 v55, v60, v61
	v_cvt_pk_bf16_f32 v56, v62, v63
	v_rcp_f32_e32 v59, v2
	v_cvt_pk_bf16_f32 v57, v64, v65
	v_lshl_add_u64 v[60:61], v[70:71], 0, v[208:209]
	v_mul_f32_e32 v2, 0xbfb8aa3b, v52
	global_store_dwordx4 v[60:61], v[54:57], off nt
	v_exp_f32_e32 v2, v2
	v_pk_mul_f32 v[50:51], v[50:51], v[58:59]
	v_mul_f32_e32 v54, 0xbfb8aa3b, v53
	v_exp_f32_e32 v54, v54
	v_add_f32_e32 v2, 1.0, v2
	v_pk_mul_f32 v[42:43], v[42:43], v[50:51]
	v_rcp_f32_e32 v50, v2
	v_add_f32_e32 v2, 1.0, v54
	v_rcp_f32_e32 v51, v2
	v_mul_f32_e32 v2, 0xbfb8aa3b, v46
	v_exp_f32_e32 v2, v2
	v_mul_f32_e32 v54, 0xbfb8aa3b, v47
	v_exp_f32_e32 v54, v54
	v_pk_mul_f32 v[50:51], v[52:53], v[50:51]
	v_add_f32_e32 v2, 1.0, v2
	v_mul_f32_e32 v53, 0xbfb8aa3b, v48
	v_rcp_f32_e32 v52, v2
	v_add_f32_e32 v2, 1.0, v54
	v_exp_f32_e32 v54, v53
	v_mul_f32_e32 v53, 0xbfb8aa3b, v49
	v_exp_f32_e32 v55, v53
	v_rcp_f32_e32 v53, v2
	v_add_f32_e32 v2, 1.0, v54
	v_rcp_f32_e32 v54, v2
	v_add_f32_e32 v2, 1.0, v55
	v_rcp_f32_e32 v55, v2
	v_pk_mul_f32 v[46:47], v[46:47], v[52:53]
	v_mul_f32_e32 v2, 0xbfb8aa3b, v34
	v_pk_mul_f32 v[46:47], v[38:39], v[46:47]
	v_pk_mul_f32 v[38:39], v[48:49], v[54:55]
	v_exp_f32_e32 v2, v2
	v_pk_mul_f32 v[48:49], v[40:41], v[38:39]
	v_mul_f32_e32 v39, 0xbfb8aa3b, v35
	v_exp_f32_e32 v40, v39
	v_add_f32_e32 v2, 1.0, v2
	v_pk_mul_f32 v[44:45], v[44:45], v[50:51]
	v_cvt_pk_bf16_f32 v38, v42, v43
	v_rcp_f32_e32 v42, v2
	v_add_f32_e32 v2, 1.0, v40
	v_cvt_pk_bf16_f32 v39, v44, v45
	v_rcp_f32_e32 v43, v2
	v_cvt_pk_bf16_f32 v40, v46, v47
	v_cvt_pk_bf16_f32 v41, v48, v49
	v_mul_f32_e32 v2, 0xbfb8aa3b, v36
	global_store_dwordx4 v[60:61], v[38:41], off offset:2048 nt
	v_exp_f32_e32 v2, v2
	v_pk_mul_f32 v[34:35], v[34:35], v[42:43]
	v_mul_f32_e32 v38, 0xbfb8aa3b, v37
	v_exp_f32_e32 v38, v38
	v_add_f32_e32 v2, 1.0, v2
	v_pk_mul_f32 v[26:27], v[26:27], v[34:35]
	v_rcp_f32_e32 v34, v2
	v_add_f32_e32 v2, 1.0, v38
	v_rcp_f32_e32 v35, v2
	v_mul_f32_e32 v2, 0xbfb8aa3b, v30
	v_exp_f32_e32 v2, v2
	v_mul_f32_e32 v38, 0xbfb8aa3b, v31
	v_exp_f32_e32 v38, v38
	v_pk_mul_f32 v[34:35], v[36:37], v[34:35]
	v_add_f32_e32 v2, 1.0, v2
	v_mul_f32_e32 v37, 0xbfb8aa3b, v32
	v_rcp_f32_e32 v36, v2
	v_add_f32_e32 v2, 1.0, v38
	v_exp_f32_e32 v38, v37
	v_mul_f32_e32 v37, 0xbfb8aa3b, v33
	v_exp_f32_e32 v39, v37
	v_rcp_f32_e32 v37, v2
	v_add_f32_e32 v2, 1.0, v38
	v_rcp_f32_e32 v38, v2
	v_add_f32_e32 v2, 1.0, v39
	v_rcp_f32_e32 v39, v2
	v_pk_mul_f32 v[30:31], v[30:31], v[36:37]
	v_mul_f32_e32 v2, 0xbfb8aa3b, v18
	v_pk_mul_f32 v[30:31], v[22:23], v[30:31]
	v_pk_mul_f32 v[22:23], v[32:33], v[38:39]
	v_exp_f32_e32 v2, v2
	v_pk_mul_f32 v[32:33], v[24:25], v[22:23]
	v_mul_f32_e32 v24, 0xbfb8aa3b, v19
	v_exp_f32_e32 v25, v24
	v_add_f32_e32 v2, 1.0, v2
	v_pk_mul_f32 v[28:29], v[28:29], v[34:35]
	v_cvt_pk_bf16_f32 v22, v26, v27
	v_rcp_f32_e32 v26, v2
	v_add_f32_e32 v2, 1.0, v25
	v_cvt_pk_bf16_f32 v23, v28, v29
	v_cvt_pk_bf16_f32 v24, v30, v31
	v_rcp_f32_e32 v27, v2
	v_cvt_pk_bf16_f32 v25, v32, v33
	v_lshl_add_u64 v[28:29], v[70:71], 0, v[210:211]
	v_mul_f32_e32 v2, 0xbfb8aa3b, v20
	global_store_dwordx4 v[28:29], v[22:25], off nt
	v_exp_f32_e32 v2, v2
	v_pk_mul_f32 v[18:19], v[18:19], v[26:27]
	v_mul_f32_e32 v22, 0xbfb8aa3b, v21
	v_exp_f32_e32 v22, v22
	v_add_f32_e32 v2, 1.0, v2
	v_pk_mul_f32 v[10:11], v[10:11], v[18:19]
	v_rcp_f32_e32 v18, v2
	v_add_f32_e32 v2, 1.0, v22
	v_rcp_f32_e32 v19, v2
	v_mul_f32_e32 v2, 0xbfb8aa3b, v14
	v_exp_f32_e32 v2, v2
	v_mul_f32_e32 v22, 0xbfb8aa3b, v15
	v_exp_f32_e32 v22, v22
	v_pk_mul_f32 v[18:19], v[20:21], v[18:19]
	v_add_f32_e32 v2, 1.0, v2
	v_mul_f32_e32 v21, 0xbfb8aa3b, v16
	v_rcp_f32_e32 v20, v2
	v_add_f32_e32 v2, 1.0, v22
	v_exp_f32_e32 v22, v21
	v_mul_f32_e32 v21, 0xbfb8aa3b, v17
	v_exp_f32_e32 v23, v21
	v_rcp_f32_e32 v21, v2
	v_add_f32_e32 v2, 1.0, v22
	v_rcp_f32_e32 v22, v2
	v_add_f32_e32 v2, 1.0, v23
	v_rcp_f32_e32 v23, v2
	v_pk_mul_f32 v[14:15], v[14:15], v[20:21]
	v_pk_mul_f32 v[12:13], v[12:13], v[18:19]
	v_pk_mul_f32 v[14:15], v[6:7], v[14:15]
	v_pk_mul_f32 v[6:7], v[16:17], v[22:23]
	s_and_b64 vcc, exec, s[0:1]
	v_pk_mul_f32 v[16:17], v[8:9], v[6:7]
	v_cvt_pk_bf16_f32 v6, v10, v11
	v_cvt_pk_bf16_f32 v7, v12, v13
	v_cvt_pk_bf16_f32 v8, v14, v15
	v_cvt_pk_bf16_f32 v9, v16, v17
	v_lshl_add_u64 v[10:11], v[70:71], 0, v[212:213]
	s_mov_b64 s[0:1], -1
	global_store_dwordx4 v[10:11], v[6:9], off nt
	s_cbranch_vccnz .LBB0_999
	s_andn2_b64 vcc, exec, s[2:3]
	s_cbranch_vccnz .LBB0_998
	s_barrier
	s_branch .LBB0_998

; __device__ __forceinline__ float wave_sum(float v) { WAVE_ALLREDUCE(op_add) return v; }
; __device__ __forceinline__ float silu_fast(float v) { return v * __builtin_amdgcn_rcpf(1.f + __builtin_amdgcn_exp2f(-1.4426950408889634f * v)); }
; __device__ __forceinline__ u32x4 pack8(const f32x4 a, const f32x4 b) { u32x4 w; w.x = cvt_pk_bf16(a[0], a[1]); w.y = cvt_pk_bf16(a[2], a[3]); w.z = cvt_pk_bf16(b[0], b[1]); w.w = cvt_pk_bf16(b[2], b[3]); return w; }
; __device__ __forceinline__ void ph_retout(const int vc, const Params& p) {
;     ...
;     for (int it = it0; it < ML * 4; it += its) {
;         const size_t o = off_of(it);
;         const u32x4 a = an, bq = bn, g = gn;
;         { const size_t on = off_of(it + its < ML * 4 ? it + its : it);
;           an = __builtin_nontemporal_load((const u32x4*)(Ob + on)); bn = __builtin_nontemporal_load((const u32x4*)(Ob + (size_t)ML * 2048 + on)); gn = __builtin_nontemporal_load((const u32x4*)(Gs + on)); }
;         const f32x4 s0 = {__uint_as_float(a.x << 16) + __uint_as_float(bq.x << 16), __uint_as_float(a.x & 0xffff0000u) + __uint_as_float(bq.x & 0xffff0000u),
;                           __uint_as_float(a.y << 16) + __uint_as_float(bq.y << 16), __uint_as_float(a.y & 0xffff0000u) + __uint_as_float(bq.y & 0xffff0000u)};
;         const f32x4 s1 = {__uint_as_float(a.z << 16) + __uint_as_float(bq.z << 16), __uint_as_float(a.z & 0xffff0000u) + __uint_as_float(bq.z & 0xffff0000u),
;                           __uint_as_float(a.w << 16) + __uint_as_float(bq.w << 16), __uint_as_float(a.w & 0xffff0000u) + __uint_as_float(bq.w & 0xffff0000u)};
;         const float ss = (s0[0] * s0[0] + s0[1] * s0[1]) + (s0[2] * s0[2] + s0[3] * s0[3]) + (s1[0] * s1[0] + s1[1] * s1[1]) + (s1[2] * s1[2] + s1[3] * s1[3]);
;         const float r = rsqrtf(wave_sum(ss) * (1.f / 512.f) + EPS);
;         f32x4 g0 = {__uint_as_float(g.x << 16), __uint_as_float(g.x & 0xffff0000u), __uint_as_float(g.y << 16), __uint_as_float(g.y & 0xffff0000u)};
;         f32x4 g1 = {__uint_as_float(g.z << 16), __uint_as_float(g.z & 0xffff0000u), __uint_as_float(g.w << 16), __uint_as_float(g.w & 0xffff0000u)};
; #pragma unroll
;         for (int j = 0; j < 4; ++j) { g0[j] = silu_fast(g0[j]); g1[j] = silu_fast(g1[j]); }
;         *(u32x4*)(WSP(bf16_t, OFF_A2B) + o) = pg8::pack8(g0 * s0 * r, g1 * s1 * r);
;     }
.LBB0_1862:
	v_add_u32_e32 v19, s22, v16
	v_cmp_gt_i32_e64 s[0:1], s14, v19
	s_waitcnt vmcnt(1)
	v_lshlrev_b32_e32 v34, 16, v3
	v_and_b32_e32 v35, 0xffff0000, v3
	v_cndmask_b32_e64 v3, v16, v19, s[0:1]
	v_lshlrev_b32_e32 v30, 16, v2
	v_and_b32_e32 v31, 0xffff0000, v2
	v_ashrrev_i32_e32 v2, 2, v3
	v_lshlrev_b32_e32 v32, 16, v4
	v_and_b32_e32 v33, 0xffff0000, v4
	v_lshlrev_b32_e32 v4, 9, v3
	v_ashrrev_i32_e32 v3, 31, v2
	v_and_or_b32 v4, v4, s15, v1
	v_lshlrev_b64 v[2:3], 12, v[2:3]
	s_waitcnt vmcnt(0)
	v_lshlrev_b32_e32 v22, 16, v10
	v_and_b32_e32 v23, 0xffff0000, v10
	v_lshlrev_b32_e32 v24, 16, v6
	v_and_b32_e32 v25, 0xffff0000, v6
	v_lshlrev_b32_e32 v10, 16, v11
	v_and_b32_e32 v11, 0xffff0000, v11
	v_lshlrev_b32_e32 v6, 16, v7
	v_and_b32_e32 v7, 0xffff0000, v7
	v_lshl_or_b32 v2, v4, 1, v2
	v_lshlrev_b32_e32 v26, 16, v12
	v_and_b32_e32 v27, 0xffff0000, v12
	v_lshlrev_b32_e32 v28, 16, v8
	v_and_b32_e32 v29, 0xffff0000, v8
	v_lshlrev_b32_e32 v12, 16, v13
	v_and_b32_e32 v13, 0xffff0000, v13
	v_lshlrev_b32_e32 v8, 16, v9
	v_and_b32_e32 v9, 0xffff0000, v9
	v_lshlrev_b32_e32 v36, 16, v5
	v_and_b32_e32 v37, 0xffff0000, v5
	v_pk_add_f32 v[22:23], v[22:23], v[24:25]
	v_pk_add_f32 v[24:25], v[10:11], v[6:7]
	v_lshl_add_u64 v[4:5], s[6:7], 0, v[2:3]
	v_lshl_add_u64 v[6:7], s[8:9], 0, v[2:3]
	v_lshl_add_u64 v[2:3], s[16:17], 0, v[2:3]
	v_pk_add_f32 v[26:27], v[26:27], v[28:29]
	v_pk_add_f32 v[28:29], v[12:13], v[8:9]
	global_load_dwordx4 v[10:13], v[4:5], off nt
	s_nop 0
	global_load_dwordx4 v[6:9], v[6:7], off nt
	s_nop 0
	global_load_dwordx4 v[2:5], v[2:3], off nt
	v_ashrrev_i32_e32 v20, 2, v16
	v_ashrrev_i32_e32 v21, 31, v20
	v_pk_mul_f32 v[38:39], v[22:23], v[22:23]
	v_pk_mul_f32 v[40:41], v[24:25], v[24:25]
	v_and_or_b32 v14, v17, s15, v1
	v_pk_mul_f32 v[42:43], v[26:27], v[26:27]
	v_lshlrev_b64 v[20:21], 12, v[20:21]
	v_add_f32_e32 v40, v40, v41
	v_add_f32_e32 v38, v38, v39
	v_lshlrev_b32_e32 v14, 1, v14
	v_pk_mul_f32 v[44:45], v[28:29], v[28:29]
	v_add_f32_e32 v41, v42, v43
	v_lshl_add_u64 v[20:21], s[10:11], 0, v[20:21]
	v_add_f32_e32 v40, v38, v40
	v_mul_f32_e32 v46, 0xbfb8aa3b, v30
	v_add_f32_e32 v44, v44, v45
	v_lshl_add_u64 v[38:39], v[20:21], 0, v[14:15]
	v_add_f32_e32 v14, v41, v40
	v_cmp_lt_i32_e32 vcc, s19, v19
	v_mov_b32_e32 v16, v19
	v_exp_f32_e32 v19, v46
	v_add_f32_e32 v14, v44, v14
	v_mul_f32_e32 v47, 0xbfb8aa3b, v31
	v_mul_f32_e32 v48, 0xbfb8aa3b, v32
	v_add_f32_dpp v14, v14, v14 quad_perm:[1,0,3,2] row_mask:0xf bank_mask:0xf bound_ctrl:1
	v_add_f32_e32 v19, 1.0, v19
	v_rcp_f32_e32 v20, v19
	v_add_f32_dpp v14, v14, v14 quad_perm:[2,3,0,1] row_mask:0xf bank_mask:0xf bound_ctrl:1
	v_mul_f32_e32 v49, 0xbfb8aa3b, v33
	v_mul_f32_e32 v50, 0xbfb8aa3b, v34
	v_add_f32_dpp v14, v14, v14 row_half_mirror row_mask:0xf bank_mask:0xf bound_ctrl:1
	v_mul_f32_e32 v51, 0xbfb8aa3b, v35
	v_mul_f32_e32 v52, 0xbfb8aa3b, v36
	v_add_f32_dpp v14, v14, v14 row_mirror row_mask:0xf bank_mask:0xf bound_ctrl:1
	v_mov_b32_e32 v19, v14
	s_nop 1
	v_permlane16_swap_b32_e32 v14, v19
	v_add_f32_e32 v14, v14, v19
	v_mul_f32_e32 v53, 0xbfb8aa3b, v37
	v_mov_b32_e32 v19, v14
	v_exp_f32_e32 v46, v47
	v_exp_f32_e32 v47, v48
	v_exp_f32_e32 v48, v49
	v_exp_f32_e32 v49, v50
	v_exp_f32_e32 v50, v51
	v_exp_f32_e32 v51, v52
	v_exp_f32_e32 v52, v53
	v_permlane32_swap_b32_e32 v14, v19
	v_add_f32_e32 v14, v14, v19
	v_fmamk_f32 v14, v14, 0x3b000000, v18
	s_or_b64 s[12:13], vcc, s[12:13]
	v_mul_f32_e32 v19, 0x4b800000, v14
	v_cmp_gt_f32_e32 vcc, s20, v14
	v_add_f32_e32 v21, 1.0, v46
	v_add_f32_e32 v40, 1.0, v47
	v_add_f32_e32 v41, 1.0, v48
	v_add_f32_e32 v42, 1.0, v49
	v_add_f32_e32 v43, 1.0, v50
	v_add_f32_e32 v44, 1.0, v51
	v_add_f32_e32 v45, 1.0, v52
	v_cndmask_b32_e32 v14, v14, v19, vcc
	v_rcp_f32_e32 v21, v21
	v_rcp_f32_e32 v40, v40
	v_rcp_f32_e32 v41, v41
	v_rcp_f32_e32 v42, v42
	v_rcp_f32_e32 v43, v43
	v_rcp_f32_e32 v44, v44
	v_rcp_f32_e32 v45, v45
	v_rsq_f32_e32 v14, v14
	v_pk_mul_f32 v[20:21], v[20:21], v[30:31]
	v_pk_mul_f32 v[30:31], v[42:43], v[34:35]
	v_pk_mul_f32 v[32:33], v[40:41], v[32:33]
	v_pk_mul_f32 v[34:35], v[44:45], v[36:37]
	v_mul_f32_e32 v19, 0x45800000, v14
	v_pk_mul_f32 v[20:21], v[22:23], v[20:21]
	v_pk_mul_f32 v[22:23], v[24:25], v[30:31]
	v_pk_mul_f32 v[24:25], v[26:27], v[32:33]
	v_pk_mul_f32 v[26:27], v[28:29], v[34:35]
	v_cndmask_b32_e32 v14, v14, v19, vcc
	v_pk_mul_f32 v[22:23], v[22:23], v[14:15] op_sel_hi:[1,0]
	v_pk_mul_f32 v[20:21], v[20:21], v[14:15] op_sel_hi:[1,0]
	v_pk_mul_f32 v[26:27], v[26:27], v[14:15] op_sel_hi:[1,0]
	v_pk_mul_f32 v[24:25], v[24:25], v[14:15] op_sel_hi:[1,0]
	v_add_u32_e32 v17, s18, v17
	v_cvt_pk_bf16_f32 v20, v20, v21
	v_cvt_pk_bf16_f32 v21, v22, v23
	v_cvt_pk_bf16_f32 v22, v24, v25
	v_cvt_pk_bf16_f32 v23, v26, v27
	global_store_dwordx4 v[38:39], v[20:23], off nt
	s_andn2_b64 exec, exec, s[12:13]
	s_cbranch_execnz .LBB0_1862

; __device__ __forceinline__ float silu_fast(float v) { return v * __builtin_amdgcn_rcpf(1.f + __builtin_amdgcn_exp2f(-1.4426950408889634f * v)); }
; __device__ __forceinline__ u32x4 pack8(const f32x4 a, const f32x4 b) { u32x4 w; w.x = cvt_pk_bf16(a[0], a[1]); w.y = cvt_pk_bf16(a[2], a[3]); w.z = cvt_pk_bf16(b[0], b[1]); w.w = cvt_pk_bf16(b[2], b[3]); return w; }
;     __device__ __forceinline__ void operator()(const f32x4 (&acc)[2][2][4][2], const Unit& u, int wr, int wc, int fr, int fq) const {
;     ...
;         for (int ai = 0; ai < 2; ++ai)
; #pragma unroll
;             for (int m = 0; m < 4; ++m) { f32x4 h[2];
; #pragma unroll
;                 for (int n = 0; n < 2; ++n)
; #pragma unroll
;                     for (int j = 0; j < 4; ++j) h[n][j] = silu_fast(acc[ai][0][m][n][j]) * acc[ai][1][m][n][j];
;                 const int row = row0 + ai * HALF + m * 16;
;                 *(u32x4*)(base + ((size_t)(row >> 7) * (FF / 64) + (col0 >> 6)) * 8192 + (row & 127) * 64 + (col0 & 63)) = pack8(h[0], h[1]); }
;     }
.LBB0_2342:
	v_mul_f32_e32 v136, 0xbfb8aa3b, v126
	v_exp_f32_e32 v136, v136
	v_mul_f32_e32 v141, 0xbfb8aa3b, v127
	v_exp_f32_e32 v141, v141
	s_lshl_b32 s13, s52, 8
	v_add_f32_e32 v136, 1.0, v136
	v_rcp_f32_e32 v152, v136
	v_add_f32_e32 v136, 1.0, v141
	v_rcp_f32_e32 v153, v136
	v_mul_f32_e32 v136, 0xbfb8aa3b, v128
	v_mul_f32_e32 v141, 0xbfb8aa3b, v129
	v_exp_f32_e32 v136, v136
	v_exp_f32_e32 v141, v141
	v_pk_mul_f32 v[126:127], v[126:127], v[152:153]
	s_add_i32 s13, s13, s39
	v_pk_mul_f32 v[118:119], v[126:127], v[118:119]
	v_add_f32_e32 v126, 1.0, v136
	v_add_f32_e32 v127, 1.0, v141
	v_mul_f32_e32 v136, 0xbfb8aa3b, v122
	v_rcp_f32_e32 v126, v126
	v_rcp_f32_e32 v127, v127
	v_exp_f32_e32 v136, v136
	v_mul_f32_e32 v141, 0xbfb8aa3b, v123
	v_exp_f32_e32 v141, v141
	v_pk_mul_f32 v[126:127], v[128:129], v[126:127]
	v_add_f32_e32 v128, 1.0, v136
	v_mul_f32_e32 v136, 0xbfb8aa3b, v124
	v_add_f32_e32 v129, 1.0, v141
	v_exp_f32_e32 v136, v136
	v_mul_f32_e32 v141, 0xbfb8aa3b, v125
	v_exp_f32_e32 v141, v141
	v_rcp_f32_e32 v128, v128
	v_add_f32_e32 v136, 1.0, v136
	v_rcp_f32_e32 v129, v129
	v_rcp_f32_e32 v152, v136
	v_add_f32_e32 v136, 1.0, v141
	v_rcp_f32_e32 v153, v136
	s_lshl_b32 s2, s16, 7
	v_pk_mul_f32 v[122:123], v[122:123], v[128:129]
	s_or_b32 s2, s2, s40
	s_ashr_i32 s16, s13, 7
	v_pk_mul_f32 v[122:123], v[122:123], v[114:115]
	v_pk_mul_f32 v[114:115], v[124:125], v[152:153]
	s_ashr_i32 s3, s2, 6
	v_mad_i64_i32 v[148:149], s[18:19], s51, v163, v[138:139]
	s_mul_i32 s16, s16, 44
	v_pk_mul_f32 v[124:125], v[114:115], v[116:117]
	v_mul_f32_e32 v117, 0xbfb8aa3b, v110
	s_ashr_i32 s2, s3, 31
	s_ashr_i32 s19, s16, 31
	v_cvt_pk_bf16_f32 v114, v118, v119
	v_exp_f32_e32 v118, v117
	v_mul_f32_e32 v117, 0xbfb8aa3b, v111
	s_add_u32 s18, s16, s3
	v_exp_f32_e32 v119, v117
	s_addc_u32 s19, s19, s2
	s_lshl_b64 s[18:19], s[18:19], 14
	v_lshl_add_u64 v[150:151], v[148:149], 0, s[18:19]
	v_pk_mul_f32 v[120:121], v[126:127], v[120:121]
	v_mov_b32_e32 v141, v137
	v_cvt_pk_bf16_f32 v115, v120, v121
	v_cvt_pk_bf16_f32 v116, v122, v123
	v_cvt_pk_bf16_f32 v117, v124, v125
	v_add_f32_e32 v118, 1.0, v118
	v_add_f32_e32 v119, 1.0, v119
	v_lshl_add_u64 v[120:121], v[150:151], 0, v[140:141]
	v_rcp_f32_e32 v118, v118
	v_rcp_f32_e32 v119, v119
	global_store_dwordx4 v[120:121], v[114:117], off nt
	v_mov_b32_e32 v143, v137
	v_mov_b32_e32 v145, v137
	v_mul_f32_e32 v114, 0xbfb8aa3b, v112
	v_mul_f32_e32 v115, 0xbfb8aa3b, v113
	v_exp_f32_e32 v114, v114
	v_exp_f32_e32 v115, v115
	v_pk_mul_f32 v[110:111], v[110:111], v[118:119]
	s_addk_i32 s13, 0x80
	v_pk_mul_f32 v[102:103], v[110:111], v[102:103]
	v_add_f32_e32 v110, 1.0, v114
	v_add_f32_e32 v111, 1.0, v115
	v_mul_f32_e32 v114, 0xbfb8aa3b, v106
	v_mul_f32_e32 v115, 0xbfb8aa3b, v107
	v_rcp_f32_e32 v110, v110
	v_rcp_f32_e32 v111, v111
	v_exp_f32_e32 v114, v114
	v_exp_f32_e32 v115, v115
	s_ashr_i32 s13, s13, 7
	v_pk_mul_f32 v[110:111], v[112:113], v[110:111]
	v_add_f32_e32 v112, 1.0, v114
	v_add_f32_e32 v113, 1.0, v115
	v_mul_f32_e32 v114, 0xbfb8aa3b, v108
	v_mul_f32_e32 v115, 0xbfb8aa3b, v109
	v_exp_f32_e32 v114, v114
	v_exp_f32_e32 v115, v115
	v_rcp_f32_e32 v112, v112
	v_rcp_f32_e32 v113, v113
	v_add_f32_e32 v114, 1.0, v114
	v_add_f32_e32 v115, 1.0, v115
	v_rcp_f32_e32 v114, v114
	v_rcp_f32_e32 v115, v115
	v_pk_mul_f32 v[106:107], v[106:107], v[112:113]
	v_pk_mul_f32 v[104:105], v[110:111], v[104:105]
	v_pk_mul_f32 v[106:107], v[106:107], v[98:99]
	v_pk_mul_f32 v[98:99], v[108:109], v[114:115]
	s_mul_i32 s13, s13, 44
	v_pk_mul_f32 v[108:109], v[98:99], v[100:101]
	v_mul_f32_e32 v99, 0xbfb8aa3b, v94
	v_exp_f32_e32 v100, v99
	v_mul_f32_e32 v99, 0xbfb8aa3b, v95
	v_exp_f32_e32 v101, v99
	v_cvt_pk_bf16_f32 v98, v102, v103
	v_add_f32_e32 v100, 1.0, v100
	v_rcp_f32_e32 v102, v100
	v_add_f32_e32 v100, 1.0, v101
	v_cvt_pk_bf16_f32 v99, v104, v105
	v_rcp_f32_e32 v103, v100
	v_cvt_pk_bf16_f32 v100, v106, v107
	v_cvt_pk_bf16_f32 v101, v108, v109
	global_store_dwordx4 v[120:121], v[98:101], off offset:2048 nt
	v_pk_mul_f32 v[94:95], v[94:95], v[102:103]
	s_ashr_i32 s16, s13, 31
	v_mul_f32_e32 v98, 0xbfb8aa3b, v96
	v_mul_f32_e32 v99, 0xbfb8aa3b, v97
	v_exp_f32_e32 v98, v98
	v_exp_f32_e32 v99, v99
	v_pk_mul_f32 v[86:87], v[94:95], v[86:87]
	s_add_u32 s18, s13, s3
	v_add_f32_e32 v94, 1.0, v98
	v_add_f32_e32 v95, 1.0, v99
	v_mul_f32_e32 v98, 0xbfb8aa3b, v90
	v_mul_f32_e32 v99, 0xbfb8aa3b, v91
	v_rcp_f32_e32 v94, v94
	v_rcp_f32_e32 v95, v95
	v_exp_f32_e32 v98, v98
	v_exp_f32_e32 v99, v99
	s_addc_u32 s19, s16, s2
	v_pk_mul_f32 v[94:95], v[96:97], v[94:95]
	v_add_f32_e32 v96, 1.0, v98
	v_add_f32_e32 v97, 1.0, v99
	v_mul_f32_e32 v98, 0xbfb8aa3b, v92
	v_mul_f32_e32 v99, 0xbfb8aa3b, v93
	v_exp_f32_e32 v98, v98
	v_exp_f32_e32 v99, v99
	v_rcp_f32_e32 v96, v96
	v_rcp_f32_e32 v97, v97
	v_add_f32_e32 v98, 1.0, v98
	v_add_f32_e32 v99, 1.0, v99
	v_rcp_f32_e32 v98, v98
	v_rcp_f32_e32 v99, v99
	v_pk_mul_f32 v[90:91], v[90:91], v[96:97]
	v_pk_mul_f32 v[88:89], v[94:95], v[88:89]
	v_pk_mul_f32 v[90:91], v[90:91], v[82:83]
	v_pk_mul_f32 v[82:83], v[92:93], v[98:99]
	s_lshl_b64 s[2:3], s[18:19], 14
	v_pk_mul_f32 v[92:93], v[82:83], v[84:85]
	v_mul_f32_e32 v85, 0xbfb8aa3b, v78
	v_cvt_pk_bf16_f32 v82, v86, v87
	v_exp_f32_e32 v86, v85
	v_mul_f32_e32 v85, 0xbfb8aa3b, v79
	v_exp_f32_e32 v87, v85
	v_cvt_pk_bf16_f32 v83, v88, v89
	v_cvt_pk_bf16_f32 v84, v90, v91
	v_cvt_pk_bf16_f32 v85, v92, v93
	v_add_f32_e32 v86, 1.0, v86
	v_add_f32_e32 v87, 1.0, v87
	v_lshl_add_u64 v[88:89], v[150:151], 0, v[142:143]
	v_rcp_f32_e32 v86, v86
	v_rcp_f32_e32 v87, v87
	global_store_dwordx4 v[88:89], v[82:85], off nt
	s_and_b64 vcc, exec, s[0:1]
	s_mov_b64 s[0:1], -1
	v_mul_f32_e32 v82, 0xbfb8aa3b, v80
; __device__ __forceinline__ float silu_fast(float v) { return v * __builtin_amdgcn_rcpf(1.f + __builtin_amdgcn_exp2f(-1.4426950408889634f * v)); }
; __device__ __forceinline__ u32x4 pack8(const f32x4 a, const f32x4 b) { u32x4 w; w.x = cvt_pk_bf16(a[0], a[1]); w.y = cvt_pk_bf16(a[2], a[3]); w.z = cvt_pk_bf16(b[0], b[1]); w.w = cvt_pk_bf16(b[2], b[3]); return w; }
;     __device__ __forceinline__ void operator()(const f32x4 (&acc)[2][2][4][2], const Unit& u, int wr, int wc, int fr, int fq) const {
;     ...
;         for (int ai = 0; ai < 2; ++ai)
; #pragma unroll
;             for (int m = 0; m < 4; ++m) { f32x4 h[2];
; #pragma unroll
;                 for (int n = 0; n < 2; ++n)
; #pragma unroll
;                     for (int j = 0; j < 4; ++j) h[n][j] = silu_fast(acc[ai][0][m][n][j]) * acc[ai][1][m][n][j];
;                 const int row = row0 + ai * HALF + m * 16;
;                 *(u32x4*)(base + ((size_t)(row >> 7) * (FF / 64) + (col0 >> 6)) * 8192 + (row & 127) * 64 + (col0 & 63)) = pack8(h[0], h[1]); }
;     }
	v_mul_f32_e32 v83, 0xbfb8aa3b, v81
	v_exp_f32_e32 v82, v82
	v_exp_f32_e32 v83, v83
	v_pk_mul_f32 v[78:79], v[78:79], v[86:87]
	s_nop 0
	v_pk_mul_f32 v[70:71], v[78:79], v[70:71]
	v_add_f32_e32 v78, 1.0, v82
	v_add_f32_e32 v79, 1.0, v83
	v_mul_f32_e32 v82, 0xbfb8aa3b, v74
	v_mul_f32_e32 v83, 0xbfb8aa3b, v75
	v_rcp_f32_e32 v78, v78
	v_rcp_f32_e32 v79, v79
	v_exp_f32_e32 v82, v82
	v_exp_f32_e32 v83, v83
	v_pk_mul_f32 v[78:79], v[80:81], v[78:79]
	v_add_f32_e32 v80, 1.0, v82
	v_add_f32_e32 v81, 1.0, v83
	v_mul_f32_e32 v82, 0xbfb8aa3b, v76
	v_mul_f32_e32 v83, 0xbfb8aa3b, v77
	v_exp_f32_e32 v82, v82
	v_exp_f32_e32 v83, v83
	v_rcp_f32_e32 v80, v80
	v_rcp_f32_e32 v81, v81
	v_add_f32_e32 v82, 1.0, v82
	v_add_f32_e32 v83, 1.0, v83
	v_rcp_f32_e32 v82, v82
	v_rcp_f32_e32 v83, v83
	v_pk_mul_f32 v[74:75], v[74:75], v[80:81]
	v_pk_mul_f32 v[72:73], v[78:79], v[72:73]
	v_pk_mul_f32 v[74:75], v[74:75], v[66:67]
	v_pk_mul_f32 v[66:67], v[76:77], v[82:83]
	s_nop 0
	v_pk_mul_f32 v[76:77], v[66:67], v[68:69]
	v_cvt_pk_bf16_f32 v66, v70, v71
	v_cvt_pk_bf16_f32 v67, v72, v73
	v_cvt_pk_bf16_f32 v68, v74, v75
	v_cvt_pk_bf16_f32 v69, v76, v77
	v_lshl_add_u64 v[70:71], v[150:151], 0, v[144:145]
	global_store_dwordx4 v[70:71], v[66:69], off nt
	s_nop 1
	v_mul_f32_e32 v66, 0xbfb8aa3b, v62
	v_exp_f32_e32 v66, v66
	v_mul_f32_e32 v67, 0xbfb8aa3b, v63
	v_exp_f32_e32 v67, v67
	v_add_f32_e32 v66, 1.0, v66
	v_rcp_f32_e32 v68, v66
	v_add_f32_e32 v66, 1.0, v67
	v_rcp_f32_e32 v69, v66
	v_lshl_add_u64 v[66:67], v[148:149], 0, s[2:3]
	v_pk_mul_f32 v[62:63], v[62:63], v[68:69]
	v_mul_f32_e32 v68, 0xbfb8aa3b, v64
	v_mul_f32_e32 v69, 0xbfb8aa3b, v65
	v_exp_f32_e32 v68, v68
	v_exp_f32_e32 v69, v69
	v_pk_mul_f32 v[54:55], v[62:63], v[54:55]
	v_add_f32_e32 v62, 1.0, v68
	v_add_f32_e32 v63, 1.0, v69
	v_mul_f32_e32 v68, 0xbfb8aa3b, v58
	v_mul_f32_e32 v69, 0xbfb8aa3b, v59
	v_rcp_f32_e32 v62, v62
	v_rcp_f32_e32 v63, v63
	v_exp_f32_e32 v68, v68
	v_exp_f32_e32 v69, v69
	v_pk_mul_f32 v[62:63], v[64:65], v[62:63]
	v_add_f32_e32 v64, 1.0, v68
	v_add_f32_e32 v65, 1.0, v69
	v_mul_f32_e32 v68, 0xbfb8aa3b, v60
	v_mul_f32_e32 v69, 0xbfb8aa3b, v61
	v_exp_f32_e32 v68, v68
	v_exp_f32_e32 v69, v69
	v_rcp_f32_e32 v64, v64
	v_rcp_f32_e32 v65, v65
	v_add_f32_e32 v68, 1.0, v68
	v_add_f32_e32 v69, 1.0, v69
	v_rcp_f32_e32 v68, v68
	v_rcp_f32_e32 v69, v69
	v_pk_mul_f32 v[58:59], v[58:59], v[64:65]
	v_pk_mul_f32 v[56:57], v[62:63], v[56:57]
	v_pk_mul_f32 v[58:59], v[58:59], v[50:51]
	v_pk_mul_f32 v[50:51], v[60:61], v[68:69]
	s_nop 0
	v_pk_mul_f32 v[60:61], v[50:51], v[52:53]
	v_mul_f32_e32 v52, 0xbfb8aa3b, v46
	v_exp_f32_e32 v53, v52
	v_mul_f32_e32 v52, 0xbfb8aa3b, v47
	v_cvt_pk_bf16_f32 v50, v54, v55
	v_exp_f32_e32 v55, v52
	v_add_f32_e32 v53, 1.0, v53
	v_rcp_f32_e32 v54, v53
	v_cvt_pk_bf16_f32 v51, v56, v57
	v_add_f32_e32 v53, 1.0, v55
	v_cvt_pk_bf16_f32 v52, v58, v59
	v_rcp_f32_e32 v55, v53
	v_cvt_pk_bf16_f32 v53, v60, v61
	v_lshl_add_u64 v[56:57], v[66:67], 0, v[140:141]
	global_store_dwordx4 v[56:57], v[50:53], off nt
	v_pk_mul_f32 v[46:47], v[46:47], v[54:55]
	s_nop 0
	v_mul_f32_e32 v50, 0xbfb8aa3b, v48
	v_mul_f32_e32 v51, 0xbfb8aa3b, v49
	v_exp_f32_e32 v50, v50
	v_exp_f32_e32 v51, v51
	v_pk_mul_f32 v[38:39], v[46:47], v[38:39]
	v_add_f32_e32 v46, 1.0, v50
	v_add_f32_e32 v47, 1.0, v51
	v_mul_f32_e32 v50, 0xbfb8aa3b, v42
	v_mul_f32_e32 v51, 0xbfb8aa3b, v43
	v_rcp_f32_e32 v46, v46
	v_rcp_f32_e32 v47, v47
	v_exp_f32_e32 v50, v50
	v_exp_f32_e32 v51, v51
	v_pk_mul_f32 v[46:47], v[48:49], v[46:47]
	v_add_f32_e32 v48, 1.0, v50
	v_add_f32_e32 v49, 1.0, v51
	v_mul_f32_e32 v50, 0xbfb8aa3b, v44
	v_mul_f32_e32 v51, 0xbfb8aa3b, v45
	v_exp_f32_e32 v50, v50
	v_exp_f32_e32 v51, v51
; __device__ __forceinline__ float silu_fast(float v) { return v * __builtin_amdgcn_rcpf(1.f + __builtin_amdgcn_exp2f(-1.4426950408889634f * v)); }
; __device__ __forceinline__ u32x4 pack8(const f32x4 a, const f32x4 b) { u32x4 w; w.x = cvt_pk_bf16(a[0], a[1]); w.y = cvt_pk_bf16(a[2], a[3]); w.z = cvt_pk_bf16(b[0], b[1]); w.w = cvt_pk_bf16(b[2], b[3]); return w; }
;     __device__ __forceinline__ void operator()(const f32x4 (&acc)[2][2][4][2], const Unit& u, int wr, int wc, int fr, int fq) const {
;     ...
;         for (int ai = 0; ai < 2; ++ai)
; #pragma unroll
;             for (int m = 0; m < 4; ++m) { f32x4 h[2];
; #pragma unroll
;                 for (int n = 0; n < 2; ++n)
; #pragma unroll
;                     for (int j = 0; j < 4; ++j) h[n][j] = silu_fast(acc[ai][0][m][n][j]) * acc[ai][1][m][n][j];
;                 const int row = row0 + ai * HALF + m * 16;
;                 *(u32x4*)(base + ((size_t)(row >> 7) * (FF / 64) + (col0 >> 6)) * 8192 + (row & 127) * 64 + (col0 & 63)) = pack8(h[0], h[1]); }
;     }
	v_rcp_f32_e32 v48, v48
	v_rcp_f32_e32 v49, v49
	v_add_f32_e32 v50, 1.0, v50
	v_add_f32_e32 v51, 1.0, v51
	v_rcp_f32_e32 v50, v50
	v_rcp_f32_e32 v51, v51
	v_pk_mul_f32 v[42:43], v[42:43], v[48:49]
	v_pk_mul_f32 v[40:41], v[46:47], v[40:41]
	v_pk_mul_f32 v[42:43], v[42:43], v[34:35]
	v_pk_mul_f32 v[34:35], v[44:45], v[50:51]
	s_nop 0
	v_pk_mul_f32 v[44:45], v[34:35], v[36:37]
	v_mul_f32_e32 v35, 0xbfb8aa3b, v30
	v_exp_f32_e32 v36, v35
	v_mul_f32_e32 v35, 0xbfb8aa3b, v31
	v_exp_f32_e32 v37, v35
	v_cvt_pk_bf16_f32 v34, v38, v39
	v_add_f32_e32 v36, 1.0, v36
	v_rcp_f32_e32 v38, v36
	v_add_f32_e32 v36, 1.0, v37
	v_cvt_pk_bf16_f32 v35, v40, v41
	v_rcp_f32_e32 v39, v36
	v_cvt_pk_bf16_f32 v36, v42, v43
	v_cvt_pk_bf16_f32 v37, v44, v45
	global_store_dwordx4 v[56:57], v[34:37], off offset:2048 nt
	v_pk_mul_f32 v[30:31], v[30:31], v[38:39]
	s_nop 0
	v_mul_f32_e32 v34, 0xbfb8aa3b, v32
	v_mul_f32_e32 v35, 0xbfb8aa3b, v33
	v_exp_f32_e32 v34, v34
	v_exp_f32_e32 v35, v35
	v_pk_mul_f32 v[22:23], v[30:31], v[22:23]
	v_add_f32_e32 v30, 1.0, v34
	v_add_f32_e32 v31, 1.0, v35
	v_mul_f32_e32 v34, 0xbfb8aa3b, v26
	v_mul_f32_e32 v35, 0xbfb8aa3b, v27
	v_rcp_f32_e32 v30, v30
	v_rcp_f32_e32 v31, v31
	v_exp_f32_e32 v34, v34
	v_exp_f32_e32 v35, v35
	v_pk_mul_f32 v[30:31], v[32:33], v[30:31]
	v_add_f32_e32 v32, 1.0, v34
	v_add_f32_e32 v33, 1.0, v35
	v_mul_f32_e32 v34, 0xbfb8aa3b, v28
	v_mul_f32_e32 v35, 0xbfb8aa3b, v29
	v_exp_f32_e32 v34, v34
	v_exp_f32_e32 v35, v35
	v_rcp_f32_e32 v32, v32
	v_rcp_f32_e32 v33, v33
	v_add_f32_e32 v34, 1.0, v34
	v_add_f32_e32 v35, 1.0, v35
	v_rcp_f32_e32 v34, v34
	v_rcp_f32_e32 v35, v35
	v_pk_mul_f32 v[26:27], v[26:27], v[32:33]
	v_pk_mul_f32 v[24:25], v[30:31], v[24:25]
	v_pk_mul_f32 v[26:27], v[26:27], v[18:19]
	v_pk_mul_f32 v[18:19], v[28:29], v[34:35]
	s_nop 0
	v_pk_mul_f32 v[28:29], v[18:19], v[20:21]
	v_mul_f32_e32 v20, 0xbfb8aa3b, v14
	v_exp_f32_e32 v21, v20
	v_mul_f32_e32 v20, 0xbfb8aa3b, v15
	v_cvt_pk_bf16_f32 v18, v22, v23
	v_exp_f32_e32 v23, v20
	v_add_f32_e32 v21, 1.0, v21
	v_rcp_f32_e32 v22, v21
	v_cvt_pk_bf16_f32 v19, v24, v25
	v_add_f32_e32 v21, 1.0, v23
	v_cvt_pk_bf16_f32 v20, v26, v27
	v_rcp_f32_e32 v23, v21
	v_cvt_pk_bf16_f32 v21, v28, v29
	v_lshl_add_u64 v[24:25], v[66:67], 0, v[142:143]
	global_store_dwordx4 v[24:25], v[18:21], off nt
	v_pk_mul_f32 v[14:15], v[14:15], v[22:23]
	s_nop 0
	v_mul_f32_e32 v18, 0xbfb8aa3b, v16
	v_mul_f32_e32 v19, 0xbfb8aa3b, v17
	v_exp_f32_e32 v18, v18
	v_exp_f32_e32 v19, v19
	v_pk_mul_f32 v[6:7], v[14:15], v[6:7]
	v_add_f32_e32 v14, 1.0, v18
	v_add_f32_e32 v15, 1.0, v19
	v_mul_f32_e32 v18, 0xbfb8aa3b, v10
	v_mul_f32_e32 v19, 0xbfb8aa3b, v11
	v_rcp_f32_e32 v14, v14
	v_rcp_f32_e32 v15, v15
	v_exp_f32_e32 v18, v18
	v_exp_f32_e32 v19, v19
	v_pk_mul_f32 v[14:15], v[16:17], v[14:15]
	v_add_f32_e32 v16, 1.0, v18
	v_add_f32_e32 v17, 1.0, v19
	v_mul_f32_e32 v18, 0xbfb8aa3b, v12
	v_mul_f32_e32 v19, 0xbfb8aa3b, v13
	v_exp_f32_e32 v18, v18
	v_exp_f32_e32 v19, v19
	v_rcp_f32_e32 v16, v16
	v_rcp_f32_e32 v17, v17
	v_add_f32_e32 v18, 1.0, v18
	v_add_f32_e32 v19, 1.0, v19
	v_rcp_f32_e32 v18, v18
	v_rcp_f32_e32 v19, v19
	v_pk_mul_f32 v[10:11], v[10:11], v[16:17]
	v_pk_mul_f32 v[8:9], v[14:15], v[8:9]
	v_pk_mul_f32 v[10:11], v[10:11], v[2:3]
	v_pk_mul_f32 v[2:3], v[12:13], v[18:19]
	s_nop 0
	v_pk_mul_f32 v[12:13], v[2:3], v[4:5]
	v_cvt_pk_bf16_f32 v2, v6, v7
	v_cvt_pk_bf16_f32 v3, v8, v9
	v_cvt_pk_bf16_f32 v4, v10, v11
	v_cvt_pk_bf16_f32 v5, v12, v13
	v_lshl_add_u64 v[6:7], v[66:67], 0, v[144:145]
	global_store_dwordx4 v[6:7], v[2:5], off nt
	s_cbranch_vccnz .LBB0_2331
	s_andn2_b64 vcc, exec, s[4:5]
	s_cbranch_vccnz .LBB0_2330
	s_barrier
	s_branch .LBB0_2330
